# baseline (speedup 1.0000x reference)
_Z11attn_kernelPKDF16_S0_S0_PKjPf:
	s_and_b32 s27, s2, 7
	s_lshr_b32 s3, s2, 3
	s_lshr_b32 s12, s2, 6
	v_readfirstlane_b32 s23, v0
	s_mov_b32 s13, 0
	s_lshl_b32 s2, s2, 5
	s_load_dwordx8 s[4:11], s[0:1], 0x0
	s_and_b32 s28, s3, 0x1ffffff8
	s_lshr_b32 s20, s23, 6
	s_lshl_b64 s[14:15], s[12:13], 11
	s_and_b32 s2, s2, 0x700
	s_or_b32 s16, s28, s27
	s_or_b32 s2, s14, s2
	s_lshl_b32 s3, s20, 5
	s_add_u32 s2, s2, s3
	s_addc_u32 s3, s15, 0
	s_lshl_b64 s[14:15], s[2:3], 10
	s_waitcnt lgkmcnt(0)
	s_add_u32 s4, s4, s14
	s_addc_u32 s5, s5, s15
	s_lshl_b32 s12, s27, 7
	s_add_u32 s4, s4, s12
	s_mov_b32 s17, s13
	s_addc_u32 s5, s5, 0
	s_lshl_b64 s[12:13], s[16:17], 18
	s_add_u32 s14, s6, s12
	s_addc_u32 s15, s7, s13
	s_add_u32 s12, s8, s12
	s_addc_u32 s13, s9, s13
	s_lshl_b32 s22, s20, 10
	s_cmp_lg_u32 0, -1
	v_and_b32_e32 v1, 63, v0
	s_cselect_b32 s6, 0, 0
	v_lshl_or_b32 v189, v1, 4, s22
	s_add_i32 s24, s22, s6
	s_mov_b32 s6, m0
	s_mov_b32 m0, s24
	s_nop 0
	global_load_lds_dwordx4 v189, s[14:15]
	s_mov_b32 m0, s6
	v_bfe_u32 v18, v0, 5, 1
	s_add_i32 s25, s24, 0x6000
	s_mov_b32 s6, m0
	s_mov_b32 m0, s25
	s_nop 0
	global_load_lds_dwordx4 v189, s[12:13]
	s_mov_b32 m0, s6
	v_and_b32_e32 v181, 31, v0
	s_add_u32 s6, s14, 0x2000
	v_lshlrev_b32_e32 v184, 4, v18
	s_addc_u32 s7, s15, 0
	s_add_i32 s17, s24, 0x2000
	s_mov_b32 s18, m0
	s_mov_b32 m0, s17
	s_nop 0
	global_load_lds_dwordx4 v189, s[6:7]
	s_mov_b32 m0, s18
	s_add_u32 s34, s14, 0x4000
	s_addc_u32 s35, s15, 0
	s_add_i32 s33, s24, 0x4000
	s_mov_b32 s36, m0
	s_mov_b32 m0, s33
	s_nop 0
	global_load_lds_dwordx4 v189, s[34:35]
	s_mov_b32 m0, s36
	v_lshl_or_b32 v2, v181, 10, v184
	global_load_dwordx4 v[124:127], v2, s[4:5]
	global_load_dwordx4 v[120:123], v2, s[4:5] offset:32
	global_load_dwordx4 v[116:119], v2, s[4:5] offset:64
	global_load_dwordx4 v[112:115], v2, s[4:5] offset:96
	v_lshlrev_b32_e32 v182, 10, v18
	v_lshlrev_b32_e32 v19, 4, v181
	v_add3_u32 v190, 0, v182, v19
	s_lshl_b32 s5, s16, 2
	s_load_dword s5, s[10:11], s5 offset:0x0
	s_mov_b32 s4, 0x42a20000
	v_mov_b32_e32 v2, 0
	v_mov_b32_e32 v3, v2
	v_mov_b32_e32 v4, v2
	v_mov_b32_e32 v5, v2
	v_mov_b32_e32 v6, v2
	v_mov_b32_e32 v7, v2
	v_mov_b32_e32 v8, v2
	v_mov_b32_e32 v9, v2
	v_mov_b32_e32 v10, v2
	v_mov_b32_e32 v11, v2
	v_mov_b32_e32 v12, v2
	v_mov_b32_e32 v13, v2
	v_mov_b32_e32 v14, v2
	v_mov_b32_e32 v15, v2
	v_mov_b32_e32 v16, v2
	v_mov_b32_e32 v17, v2
	s_waitcnt vmcnt(3)
	v_fma_mix_f32 v19, v124, v124, 0 op_sel_hi:[1,1,0]
	s_nop 0
	v_fma_mix_f32 v19, v124, v124, v19 op_sel:[1,1,0] op_sel_hi:[1,1,0]
	s_nop 0
	v_fma_mix_f32 v19, v125, v125, v19 op_sel_hi:[1,1,0]
	s_nop 0
	v_fma_mix_f32 v19, v125, v125, v19 op_sel:[1,1,0] op_sel_hi:[1,1,0]
	s_nop 0
	v_fma_mix_f32 v19, v126, v126, v19 op_sel_hi:[1,1,0]
	s_nop 0
	v_fma_mix_f32 v19, v126, v126, v19 op_sel:[1,1,0] op_sel_hi:[1,1,0]
	s_nop 0
	v_fma_mix_f32 v19, v127, v127, v19 op_sel_hi:[1,1,0]
	s_nop 0
	v_fma_mix_f32 v19, v127, v127, v19 op_sel:[1,1,0] op_sel_hi:[1,1,0]
	s_waitcnt vmcnt(2)
	v_fma_mix_f32 v19, v120, v120, v19 op_sel_hi:[1,1,0]
	s_nop 0
	v_fma_mix_f32 v19, v120, v120, v19 op_sel:[1,1,0] op_sel_hi:[1,1,0]
	s_nop 0
	v_fma_mix_f32 v19, v121, v121, v19 op_sel_hi:[1,1,0]
	s_nop 0
	v_fma_mix_f32 v19, v121, v121, v19 op_sel:[1,1,0] op_sel_hi:[1,1,0]
	s_nop 0
	v_fma_mix_f32 v19, v122, v122, v19 op_sel_hi:[1,1,0]
	s_nop 0
	v_fma_mix_f32 v19, v122, v122, v19 op_sel:[1,1,0] op_sel_hi:[1,1,0]
	s_nop 0
	v_fma_mix_f32 v19, v123, v123, v19 op_sel_hi:[1,1,0]
	s_nop 0
	v_fma_mix_f32 v19, v123, v123, v19 op_sel:[1,1,0] op_sel_hi:[1,1,0]
	s_waitcnt vmcnt(1)
	v_fma_mix_f32 v19, v116, v116, v19 op_sel_hi:[1,1,0]
	s_nop 0
	v_fma_mix_f32 v19, v116, v116, v19 op_sel:[1,1,0] op_sel_hi:[1,1,0]
	s_nop 0
	v_fma_mix_f32 v19, v117, v117, v19 op_sel_hi:[1,1,0]
	s_nop 0
	v_fma_mix_f32 v19, v117, v117, v19 op_sel:[1,1,0] op_sel_hi:[1,1,0]
	s_nop 0
	v_fma_mix_f32 v19, v118, v118, v19 op_sel_hi:[1,1,0]
	s_nop 0
	v_fma_mix_f32 v19, v118, v118, v19 op_sel:[1,1,0] op_sel_hi:[1,1,0]
	s_nop 0
	v_fma_mix_f32 v19, v119, v119, v19 op_sel_hi:[1,1,0]
	s_nop 0
	v_fma_mix_f32 v19, v119, v119, v19 op_sel:[1,1,0] op_sel_hi:[1,1,0]
	s_waitcnt vmcnt(0)
	v_fma_mix_f32 v19, v112, v112, v19 op_sel_hi:[1,1,0]
	s_nop 0
	v_fma_mix_f32 v19, v112, v112, v19 op_sel:[1,1,0] op_sel_hi:[1,1,0]
	s_nop 0
	v_fma_mix_f32 v19, v113, v113, v19 op_sel_hi:[1,1,0]
	s_nop 0
	v_fma_mix_f32 v19, v113, v113, v19 op_sel:[1,1,0] op_sel_hi:[1,1,0]
	s_nop 0
	v_fma_mix_f32 v19, v114, v114, v19 op_sel_hi:[1,1,0]
	s_nop 0
	v_fma_mix_f32 v19, v114, v114, v19 op_sel:[1,1,0] op_sel_hi:[1,1,0]
	s_nop 0
	v_fma_mix_f32 v19, v115, v115, v19 op_sel_hi:[1,1,0]
	s_nop 0
	v_fma_mix_f32 v19, v115, v115, v19 op_sel:[1,1,0] op_sel_hi:[1,1,0]
	s_nop 0
	v_mov_b32_e32 v20, v19
	s_nop 1
	v_permlane32_swap_b32_e32 v19, v20
	v_add_f32_e32 v19, v19, v20
	s_waitcnt lgkmcnt(0)
	v_mul_f32_e32 v19, s5, v19
	v_cmp_ge_f32_e32 vcc, s4, v19
	s_cmp_eq_u64 vcc, exec
	s_cselect_b64 s[4:5], -1, 0
	s_waitcnt vmcnt(3) lgkmcnt(0)
	s_barrier
	ds_read_b128 v[20:23], v190
	ds_read_b128 v[24:27], v190 offset:512
	s_waitcnt lgkmcnt(1)
	v_mfma_f32_32x32x16_f16 v[96:111], v[20:23], v[124:127], v[2:17]
	v_cndmask_b32_e64 v19, 0, 1, s[4:5]
	s_nop 0
	v_readfirstlane_b32 s4, v19
	s_bitcmp1_b32 s4, 0
	s_cselect_b64 s[16:17], -1, 0
	s_xor_b64 s[18:19], s[16:17], -1
	s_mov_b64 s[4:5], -1
	s_waitcnt lgkmcnt(0)
	v_mfma_f32_32x32x16_f16 v[80:95], v[24:27], v[124:127], v[2:17]
	ds_read_b128 v[20:23], v190 offset:2048
	ds_read_b128 v[24:27], v190 offset:2560
	s_and_b64 vcc, exec, s[18:19]
	s_waitcnt lgkmcnt(1)
	v_mfma_f32_32x32x16_f16 v[96:111], v[20:23], v[120:123], v[96:111]
	s_waitcnt lgkmcnt(0)
	v_mfma_f32_32x32x16_f16 v[80:95], v[24:27], v[120:123], v[80:95]
	ds_read_b128 v[20:23], v190 offset:4096
	ds_read_b128 v[24:27], v190 offset:4608
	s_waitcnt lgkmcnt(1)
	v_mfma_f32_32x32x16_f16 v[96:111], v[20:23], v[116:119], v[96:111]
	s_waitcnt lgkmcnt(0)
	v_mfma_f32_32x32x16_f16 v[80:95], v[24:27], v[116:119], v[80:95]
	ds_read_b128 v[20:23], v190 offset:6144
	ds_read_b128 v[24:27], v190 offset:6656
	s_waitcnt lgkmcnt(1)
	v_mfma_f32_32x32x16_f16 v[96:111], v[20:23], v[112:115], v[96:111]
	s_waitcnt lgkmcnt(0)
	v_mfma_f32_32x32x16_f16 v[80:95], v[24:27], v[112:115], v[80:95]
	s_cbranch_vccz .LBB2_2
	v_max3_f32 v19, v96, v97, v80
	v_max3_f32 v20, v98, v99, v81
	s_nop 0
	v_max3_f32 v19, v19, v82, v83
	v_max3_f32 v20, v20, v102, v103
	s_nop 0
	v_max3_f32 v19, v19, v100, v101
	v_max3_f32 v20, v20, v86, v87
	s_nop 0
	v_max3_f32 v19, v19, v84, v85
	v_max3_f32 v20, v20, v106, v107
	s_nop 0
	v_max3_f32 v19, v19, v104, v105
	v_max3_f32 v20, v20, v90, v91
	s_nop 0
	v_max3_f32 v19, v19, v88, v89
	v_max3_f32 v20, v20, v110, v111
	s_nop 0
	v_max3_f32 v19, v19, v108, v109
	v_max3_f32 v20, v20, v94, v95
	s_nop 0
	v_max3_f32 v19, v19, v92, v93
	s_nop 0
	v_max_f32 v19, v19, v20
	s_nop 0
	v_mov_b32_e32 v20, v19
	s_nop 1
	v_permlane32_swap_b32_e32 v19, v20
	v_max_f32 v180, v19, v20
	s_nop 0
	v_sub_f32_e32 v19, v96, v180
	v_exp_f32_e32 v64, v19
	v_sub_f32_e32 v19, v80, v180
	v_exp_f32_e32 v48, v19
	v_sub_f32_e32 v19, v97, v180
	v_exp_f32_e32 v65, v19
	v_sub_f32_e32 v19, v81, v180
	v_exp_f32_e32 v49, v19
	v_sub_f32_e32 v19, v98, v180
	v_exp_f32_e32 v66, v19
	v_sub_f32_e32 v19, v82, v180
	v_exp_f32_e32 v50, v19
	v_sub_f32_e32 v19, v99, v180
	v_exp_f32_e32 v67, v19
	v_sub_f32_e32 v19, v83, v180
	v_exp_f32_e32 v51, v19
	v_sub_f32_e32 v19, v100, v180
	v_exp_f32_e32 v68, v19
	v_sub_f32_e32 v19, v84, v180
	v_exp_f32_e32 v52, v19
	v_sub_f32_e32 v19, v101, v180
	v_exp_f32_e32 v69, v19
	v_sub_f32_e32 v19, v85, v180
	v_exp_f32_e32 v53, v19
	v_sub_f32_e32 v19, v102, v180
	v_exp_f32_e32 v70, v19
	v_sub_f32_e32 v19, v86, v180
	v_exp_f32_e32 v54, v19
	v_sub_f32_e32 v19, v103, v180
	v_exp_f32_e32 v71, v19
	v_sub_f32_e32 v19, v87, v180
	v_exp_f32_e32 v55, v19
	v_sub_f32_e32 v19, v104, v180
	v_exp_f32_e32 v72, v19
	v_sub_f32_e32 v19, v105, v180
	v_exp_f32_e32 v73, v19
	v_sub_f32_e32 v19, v106, v180
	v_exp_f32_e32 v74, v19
	v_sub_f32_e32 v19, v107, v180
	v_exp_f32_e32 v75, v19
	v_sub_f32_e32 v19, v108, v180
	v_exp_f32_e32 v76, v19
	v_sub_f32_e32 v19, v109, v180
	v_exp_f32_e32 v77, v19
	v_sub_f32_e32 v19, v110, v180
	v_xor_b32_e32 v32, 0x80000000, v180
	v_exp_f32_e32 v78, v19
	v_sub_f32_e32 v19, v111, v180
	v_mov_b32_e32 v33, v32
	v_mov_b32_e32 v34, v32
	v_mov_b32_e32 v35, v32
	v_mov_b32_e32 v36, v32
	v_mov_b32_e32 v37, v32
	v_mov_b32_e32 v38, v32
	v_mov_b32_e32 v39, v32
	v_mov_b32_e32 v40, v32
	v_mov_b32_e32 v41, v32
	v_mov_b32_e32 v42, v32
	v_mov_b32_e32 v43, v32
	v_mov_b32_e32 v44, v32
	v_mov_b32_e32 v45, v32
	v_mov_b32_e32 v46, v32
	v_mov_b32_e32 v47, v32
	v_pk_add_f32 v[56:57], v[88:89], v[180:181] op_sel_hi:[1,0] neg_lo:[0,1] neg_hi:[0,1]
	v_pk_add_f32 v[58:59], v[90:91], v[180:181] op_sel_hi:[1,0] neg_lo:[0,1] neg_hi:[0,1]
	v_pk_add_f32 v[60:61], v[92:93], v[180:181] op_sel_hi:[1,0] neg_lo:[0,1] neg_hi:[0,1]
	v_exp_f32_e32 v79, v19
	v_pk_add_f32 v[62:63], v[94:95], v[180:181] op_sel_hi:[1,0] neg_lo:[0,1] neg_hi:[0,1]
	s_load_dwordx2 s[6:7], s[0:1], 0x20
	s_lshl_b32 s21, s27, 6
	s_cbranch_execz .LBB2_3
	s_branch .LBB2_4
